# speedup vs baseline: 1.0050x; 1.0050x over previous
.LBB1_16:
	v_add_u32_e32 v215, 0x200, v215
	v_cmp_lt_u32_e32 vcc, s21, v215
	ds_write_b16 v213, v212
	s_or_b64 s[4:5], vcc, s[4:5]
	v_add_u32_e32 v213, 0x400, v213
	s_andn2_b64 exec, exec, s[4:5]
	s_cbranch_execnz .LBB1_16
	s_or_b64 exec, exec, s[4:5]
	s_movk_i32 s4, 0xff
	v_cmp_eq_u32_e32 vcc, s20, v214
	v_cmp_lt_u32_e64 s[4:5], s4, v162
	s_waitcnt lgkmcnt(0)
	s_barrier
	v_readfirstlane_b32 s20, v162
	s_bitcmp1_b32 s20, 8
	s_cbranch_scc0 .Lnoprio
	s_setprio 1
.Lnoprio:
	s_xor_b64 s[4:5], s[10:11], -1
	s_lshl_b64 s[28:29], s[24:25], 16
	s_cmp_eq_u64 vcc, s[12:13]
	s_cselect_b64 s[12:13], -1, 0
	s_and_b64 s[20:21], s[12:13], s[4:5]
	s_add_u32 s33, s16, s28
	s_addc_u32 s35, s17, s29
	s_mul_i32 s40, s6, s7
	s_ashr_i32 s7, s6, 31
	s_sub_i32 s41, s24, s40
	s_lshl_b64 s[4:5], s[6:7], 23
	s_add_u32 s4, s8, s4
	s_addc_u32 s5, s9, s5
	s_lshl_b32 s8, s34, 8
	s_lshl_b32 s9, s34, 10
	s_add_u32 s28, s4, s9
	s_addc_u32 s29, s5, 0
	s_lshl_b64 s[4:5], s[6:7], 21
	s_add_u32 s4, s14, s4
	s_addc_u32 s5, s15, s5
	s_lshl_b32 s42, s34, 6
	s_add_u32 s30, s4, s8
	s_addc_u32 s31, s5, 0
	v_and_b32_e32 v171, 15, v162
	s_lshl_b32 s4, s41, 6
	v_lshl_or_b32 v130, v171, 2, s4
	v_subrev_u32_e32 v201, 32, v130
	v_max_i32_e32 v130, 0, v201
	v_sub_u32_e32 v131, 0x7ff, v130
	v_cndmask_b32_e64 v130, v131, v130, s[0:1]
	v_bfe_u32 v146, v162, 4, 2
	v_ashrrev_i32_e32 v131, 31, v130
	v_or_b32_e32 v199, v137, v146
	v_lshlrev_b64 v[130:131], 12, v[130:131]
	v_or_b32_e32 v134, 4, v199
	v_lshl_add_u64 v[130:131], s[28:29], 0, v[130:131]
	v_mov_b32_e32 v167, 0
	v_lshlrev_b32_e32 v166, 4, v199
	v_lshl_add_u64 v[132:133], v[130:131], 0, v[166:167]
	v_lshlrev_b32_e32 v166, 4, v134
	v_lshl_add_u64 v[130:131], v[130:131], 0, v[166:167]
	global_load_dwordx4 v[142:145], v[130:131], off
	global_load_dwordx4 v[138:141], v[132:133], off
	v_lshlrev_b32_e32 v164, 2, v199
	v_lshlrev_b32_e32 v170, 2, v134
	v_lshlrev_b32_e32 v134, 8, v171
	s_mov_b32 s4, 0x8400
	v_add3_u32 v203, v134, v164, s4
	v_lshlrev_b32_e32 v134, 1, v1
	v_sub_u32_e32 v135, v134, v171
	v_or_b32_e32 v134, 1, v134
	v_sub_u32_e32 v134, v134, v171
	s_lshl_b32 s4, s34, 4
	v_lshlrev_b32_e32 v206, 2, v134
	v_mul_u32_u24_e32 v134, 6, v1
	s_add_i32 s4, s4, 16
	v_mad_u32_u24 v130, v1, 6, s4
	v_and_b32_e32 v131, 14, v134
	v_and_or_b32 v130, v130, 48, v131
	v_lshlrev_b32_e32 v172, 6, v130
	v_or_b32_e32 v130, 1, v134
	v_add_u32_e32 v130, s4, v130
	v_bitop3_b32 v131, v134, 15, 1 bitop3:0xc8
	v_and_or_b32 v130, v130, 48, v131
	v_lshlrev_b32_e32 v174, 6, v130
	v_mad_u32_u24 v130, v1, 6, 2
	v_add_u32_e32 v131, s4, v130
	v_and_b32_e32 v132, 14, v130
	v_and_or_b32 v131, v131, 48, v132
	v_lshlrev_b32_e32 v176, 6, v131
	v_mad_u32_u24 v131, v1, 6, 3
	v_and_b32_e32 v136, 63, v162
	v_add_u32_e32 v132, s4, v131
	v_and_b32_e32 v133, 15, v131
	v_lshlrev_b32_e32 v166, 2, v136
	v_and_or_b32 v132, v132, 48, v133
	v_lshlrev_b32_e32 v204, 2, v135
	v_lshl_or_b32 v135, v1, 9, v166
	v_lshlrev_b32_e32 v178, 6, v132
	v_mad_u32_u24 v132, v1, 6, 4
	v_add_u32_e32 v205, 0x8400, v135
	v_add_u32_e32 v133, s4, v132
	v_and_b32_e32 v135, 14, v132
	v_and_or_b32 v133, v133, 48, v135
	s_add_i32 s34, s34, 1
	v_lshrrev_b32_e32 v134, 4, v134
	v_lshl_add_u32 v184, v1, 7, s9
	v_lshlrev_b32_e32 v180, 6, v133
	v_mad_u32_u24 v133, v1, 6, 5
	v_add_lshl_u32 v134, s34, v134, 6
	v_mul_u32_u24_e32 v1, 24, v1
	v_and_b32_e32 v134, 0xc0, v134
	v_and_b32_e32 v1, 56, v1
	v_or3_b32 v183, v1, v134, v146
	v_lshrrev_b32_e32 v1, 4, v130
	v_add_lshl_u32 v1, s34, v1, 6
	v_lshlrev_b32_e32 v130, 2, v130
	v_and_b32_e32 v1, 0xc0, v1
	v_and_b32_e32 v130, 56, v130
	v_or3_b32 v185, v130, v1, v146
	v_lshrrev_b32_e32 v1, 4, v131
	v_add_lshl_u32 v1, s34, v1, 6
	v_lshlrev_b32_e32 v130, 2, v131
	v_and_b32_e32 v1, 0xc0, v1
	v_and_b32_e32 v130, 60, v130
	v_or3_b32 v192, v130, v1, v146
	v_lshrrev_b32_e32 v1, 4, v132
	v_add_lshl_u32 v1, s34, v1, 6
	v_lshlrev_b32_e32 v130, 2, v132
	v_and_b32_e32 v1, 0xc0, v1
	v_and_b32_e32 v130, 56, v130
	v_or3_b32 v193, v130, v1, v146
	v_lshrrev_b32_e32 v1, 4, v133
	v_add_u32_e32 v135, s4, v133
	v_and_b32_e32 v137, 15, v133
	v_add_lshl_u32 v1, s34, v1, 6
	v_lshlrev_b32_e32 v130, 2, v133
	v_and_or_b32 v135, v135, 48, v137
	v_and_b32_e32 v1, 0xc0, v1
	v_and_b32_e32 v130, 60, v130
	v_lshlrev_b32_e32 v182, 6, v135
	v_or3_b32 v194, v130, v1, v146
	v_lshlrev_b32_e32 v168, 3, v136
	s_waitcnt vmcnt(1)
	v_mov_b64_e32 v[130:131], v[142:143]
	s_waitcnt vmcnt(0)
	v_mov_b64_e32 v[134:135], v[138:139]
	s_mov_b32 s43, 0
	v_lshlrev_b32_e32 v173, 3, v146
	v_and_b32_e32 v200, 48, v162
	v_add_u32_e32 v181, s42, v199
	s_mov_b32 s34, 0x48800000
	s_mov_b32 s36, 0x36800000
	v_mov_b32_e32 v188, v167
	v_mov_b32_e32 v189, v167
	v_mul_u32_u24_e32 v195, 0x210, v171
	v_bfe_u32 v216, v162, 4, 1
	v_bfe_u32 v217, v162, 5, 1
	s_lshr_b32 s4, s42, 6
	s_add_i32 s4, s4, 1
	v_lshlrev_b32_e32 v218, 3, v171
	v_lshrrev_b32_e32 v219, 6, v162
	v_mad_u32_u24 v219, v219, 6, v217
	v_lshrrev_b32_e32 v220, 4, v219
	v_add_u32_e32 v220, s4, v220
	v_and_b32_e32 v220, 3, v220
	v_and_b32_e32 v221, 15, v219
	v_lshl_add_u32 v222, v220, 4, v221
	v_lshlrev_b32_e32 v223, 6, v222
	v_lshl_add_u32 v223, v216, 5, v223
	v_lshl_add_u32 v228, v223, 3, v218
	v_lshlrev_b32_e32 v223, 2, v222
	v_lshl_add_u32 v223, v216, 1, v223
	v_lshl_add_u32 v231, v223, 1, v195
	v_add_u32_e32 v219, 2, v219
	v_lshrrev_b32_e32 v220, 4, v219
	v_add_u32_e32 v220, s4, v220
	v_and_b32_e32 v220, 3, v220
	v_and_b32_e32 v221, 15, v219
	v_lshl_add_u32 v222, v220, 4, v221
	v_lshlrev_b32_e32 v223, 6, v222
	v_lshl_add_u32 v223, v216, 5, v223
	v_lshl_add_u32 v229, v223, 3, v218
	v_lshlrev_b32_e32 v223, 2, v222
	v_lshl_add_u32 v223, v216, 1, v223
	v_lshl_add_u32 v232, v223, 1, v195
	v_add_u32_e32 v219, 2, v219
	v_lshrrev_b32_e32 v220, 4, v219
	v_add_u32_e32 v220, s4, v220
	v_and_b32_e32 v220, 3, v220
	v_and_b32_e32 v221, 15, v219
	v_lshl_add_u32 v222, v220, 4, v221
	v_lshlrev_b32_e32 v223, 6, v222
	v_lshl_add_u32 v223, v216, 5, v223
	v_lshl_add_u32 v230, v223, 3, v218
	v_lshlrev_b32_e32 v223, 2, v222
	v_lshl_add_u32 v223, v216, 1, v223
	v_lshl_add_u32 v233, v223, 1, v195
	v_lshl_add_u32 v234, v184, 3, v168
	v_mov_b32_e32 v207, 1
	v_mov_b32_e32 v202, 0
	v_mov_b32_e32 v198, 0
	v_mov_b32_e32 v197, 0
	v_mov_b32_e32 v196, 0
	v_mov_b32_e32 v179, 0
	v_mov_b32_e32 v177, 0
	v_mov_b32_e32 v175, 0
	v_mov_b32_e32 v1, 0
	v_lshl_add_u64 v[186:187], s[30:31], 0, v[166:167]
	v_mov_b64_e32 v[132:133], v[144:145]
	v_mov_b64_e32 v[136:137], v[140:141]

.LBB1_22:
	s_and_b32 s12, s43, 1
	s_cmp_lt_u32 s43, 24
	s_mul_i32 s8, s12, 0x4200
	s_mov_b64 s[6:7], -1
	s_cbranch_scc1 .LBB1_24
	v_lshlrev_b32_e32 v146, 1, v173
	v_add3_u32 v166, s8, v195, v146
	ds_read_b128 v[146:149], v166
	ds_read_b128 v[150:153], v166 offset:64
	ds_read_b128 v[212:215], v166 offset:8448
	ds_read_b128 v[216:219], v166 offset:8512
	s_cmp_eq_u32 s43, 35
	s_cbranch_scc1 .Lx_skip_f
	v_max_i32_e32 v130, -1, v190
	v_add_u32_e32 v131, 1, v130
	v_sub_u32_e32 v130, 0x7fe, v130
	v_cndmask_b32_e64 v130, v130, v131, s[0:1]
	v_lshlrev_b32_e32 v130, 12, v130
	v_lshl_add_u32 v226, v164, 2, v130
	global_load_dwordx4 v[134:137], v226, s[28:29]
	global_load_dwordx4 v[130:133], v226, s[28:29] offset:64
.Lx_skip_f:
	s_waitcnt lgkmcnt(3)
	v_mfma_f32_16x16x32_f16 v[154:157], v[18:21], v[146:149], v[138:141]
	v_mfma_f32_16x16x32_f16 v[158:161], v[74:77], v[146:149], v[142:145]
	v_mfma_f32_16x16x32_f16 v[208:211], v[22:25], v[146:149], 0
	v_mfma_f32_16x16x32_f16 v[146:149], v[78:81], v[146:149], 0
	s_waitcnt lgkmcnt(1)
	v_mfma_f32_16x16x32_f16 v[208:211], v[18:21], v[212:215], v[208:211]
	v_mfma_f32_16x16x32_f16 v[146:149], v[74:77], v[212:215], v[146:149]
	v_mfma_f32_16x16x32_f16 v[208:211], v[30:33], v[150:153], v[208:211]
	v_mfma_f32_16x16x32_f16 v[146:149], v[86:89], v[150:153], v[146:149]
	v_mfma_f32_16x16x32_f16 v[154:157], v[26:29], v[150:153], v[154:157]
	v_mfma_f32_16x16x32_f16 v[158:161], v[82:85], v[150:153], v[158:161]
	s_waitcnt lgkmcnt(0)
	v_mfma_f32_16x16x32_f16 v[150:153], v[26:29], v[216:219], v[208:211]
	v_mfma_f32_16x16x32_f16 v[146:149], v[82:85], v[216:219], v[146:149]
	s_nop 1
	ds_read_b128 v[208:211], v166 offset:128
	ds_read_b128 v[212:215], v166 offset:192
	s_waitcnt lgkmcnt(1)
	v_mfma_f32_16x16x32_f16 v[154:157], v[34:37], v[208:211], v[154:157]
	v_mfma_f32_16x16x32_f16 v[158:161], v[90:93], v[208:211], v[158:161]
	v_mfma_f32_16x16x32_f16 v[150:153], v[38:41], v[208:211], v[150:153]
	v_mfma_f32_16x16x32_f16 v[146:149], v[94:97], v[208:211], v[146:149]
	ds_read_b128 v[208:211], v166 offset:8576
	ds_read_b128 v[216:219], v166 offset:8640
	s_waitcnt lgkmcnt(1)
	v_mfma_f32_16x16x32_f16 v[150:153], v[34:37], v[208:211], v[150:153]
	v_mfma_f32_16x16x32_f16 v[146:149], v[90:93], v[208:211], v[146:149]
	v_mfma_f32_16x16x32_f16 v[150:153], v[46:49], v[212:215], v[150:153]
	v_mfma_f32_16x16x32_f16 v[146:149], v[102:105], v[212:215], v[146:149]
	v_mfma_f32_16x16x32_f16 v[154:157], v[42:45], v[212:215], v[154:157]
	v_mfma_f32_16x16x32_f16 v[158:161], v[98:101], v[212:215], v[158:161]
	s_waitcnt lgkmcnt(0)
	v_mfma_f32_16x16x32_f16 v[150:153], v[42:45], v[216:219], v[150:153]
	v_mfma_f32_16x16x32_f16 v[146:149], v[98:101], v[216:219], v[146:149]
	ds_read_b128 v[208:211], v166 offset:256
	ds_read_b128 v[212:215], v166 offset:320
	s_waitcnt lgkmcnt(1)
	v_mfma_f32_16x16x32_f16 v[154:157], v[50:53], v[208:211], v[154:157]
	v_mfma_f32_16x16x32_f16 v[158:161], v[106:109], v[208:211], v[158:161]
	v_mfma_f32_16x16x32_f16 v[150:153], v[54:57], v[208:211], v[150:153]
	v_mfma_f32_16x16x32_f16 v[146:149], v[110:113], v[208:211], v[146:149]
	ds_read_b128 v[208:211], v166 offset:8704
	ds_read_b128 v[216:219], v166 offset:8768
	s_waitcnt lgkmcnt(1)
	v_mfma_f32_16x16x32_f16 v[150:153], v[50:53], v[208:211], v[150:153]
	v_mfma_f32_16x16x32_f16 v[146:149], v[106:109], v[208:211], v[146:149]
	v_mfma_f32_16x16x32_f16 v[150:153], v[62:65], v[212:215], v[150:153]
	v_mfma_f32_16x16x32_f16 v[146:149], v[118:121], v[212:215], v[146:149]
	v_mfma_f32_16x16x32_f16 v[154:157], v[58:61], v[212:215], v[154:157]
	v_mfma_f32_16x16x32_f16 v[158:161], v[114:117], v[212:215], v[158:161]
	s_waitcnt lgkmcnt(0)
	v_mfma_f32_16x16x32_f16 v[150:153], v[58:61], v[216:219], v[150:153]
	v_mfma_f32_16x16x32_f16 v[146:149], v[114:117], v[216:219], v[146:149]
	ds_read_b128 v[208:211], v166 offset:384
	ds_read_b128 v[212:215], v166 offset:448
	s_waitcnt lgkmcnt(1)
	v_mfma_f32_16x16x32_f16 v[154:157], v[66:69], v[208:211], v[154:157]
	v_mfma_f32_16x16x32_f16 v[216:219], v[122:125], v[208:211], v[158:161]
	v_mfma_f32_16x16x32_f16 v[150:153], v[70:73], v[208:211], v[150:153]
	v_mfma_f32_16x16x32_f16 v[146:149], v[126:129], v[208:211], v[146:149]
	s_nop 0
	ds_read_b128 v[158:161], v166 offset:8832
	ds_read_b128 v[208:211], v166 offset:8896
	s_waitcnt lgkmcnt(1)
	v_mfma_f32_16x16x32_f16 v[220:223], v[66:69], v[158:161], v[150:153]
	v_mfma_f32_16x16x32_f16 v[146:149], v[122:125], v[158:161], v[146:149]
	v_mfma_f32_16x16x32_f16 v[158:161], v[2:5], v[212:215], v[154:157]
	v_mfma_f32_16x16x32_f16 v[154:157], v[6:9], v[212:215], v[220:223]
	v_mfma_f32_16x16x32_f16 v[146:149], v[14:17], v[212:215], v[146:149]
	v_mfma_f32_16x16x32_f16 v[150:153], v[10:13], v[212:215], v[216:219]
	s_waitcnt lgkmcnt(0)
	v_mfma_f32_16x16x32_f16 v[154:157], v[2:5], v[208:211], v[154:157]
	v_mfma_f32_16x16x32_f16 v[146:149], v[10:13], v[208:211], v[146:149]
	s_mov_b64 s[6:7], 0
.LBB1_24:
	s_andn2_b64 vcc, exec, s[6:7]
	s_cbranch_vccnz .LBB1_26
	v_add3_u32 v166, s8, v195, v200
	s_nop 3
	ds_read_b128 v[146:149], v166
	ds_read_b128 v[150:153], v166 offset:64
	ds_read_b128 v[154:157], v166 offset:128
	ds_read_b128 v[158:161], v166 offset:192
	ds_read_b128 v[208:211], v166 offset:256
	ds_read_b128 v[212:215], v166 offset:320
	ds_read_b128 v[216:219], v166 offset:384
	ds_read_b128 v[220:223], v166 offset:448
	s_cmp_eq_u32 s43, 35
	s_cbranch_scc1 .Lx_skip_l
	v_max_i32_e32 v130, -1, v190
	v_add_u32_e32 v131, 1, v130
	v_sub_u32_e32 v130, 0x7fe, v130
	v_cndmask_b32_e64 v130, v130, v131, s[0:1]
	v_lshlrev_b32_e32 v130, 12, v130
	v_lshl_add_u32 v226, v164, 2, v130
	global_load_dwordx4 v[134:137], v226, s[28:29]
	global_load_dwordx4 v[130:133], v226, s[28:29] offset:64
.Lx_skip_l:
	s_waitcnt lgkmcnt(7)
	v_mfma_f32_16x16x32_f16 v[138:141], v[18:21], v[146:149], v[138:141]
	s_waitcnt lgkmcnt(6)
	v_mfma_f32_16x16x32_f16 v[138:141], v[26:29], v[150:153], v[138:141]
	s_waitcnt lgkmcnt(5)
	v_mfma_f32_16x16x32_f16 v[138:141], v[34:37], v[154:157], v[138:141]
	s_waitcnt lgkmcnt(4)
	v_mfma_f32_16x16x32_f16 v[138:141], v[42:45], v[158:161], v[138:141]
	s_waitcnt lgkmcnt(3)
	v_mfma_f32_16x16x32_f16 v[138:141], v[50:53], v[208:211], v[138:141]
	s_waitcnt lgkmcnt(2)
	v_mfma_f32_16x16x32_f16 v[138:141], v[58:61], v[212:215], v[138:141]
	s_waitcnt lgkmcnt(1)
	v_mfma_f32_16x16x32_f16 v[138:141], v[66:69], v[216:219], v[138:141]
	s_waitcnt lgkmcnt(0)
	v_mfma_f32_16x16x32_f16 v[138:141], v[2:5], v[220:223], v[138:141]
	v_mfma_f32_16x16x32_f16 v[142:145], v[74:77], v[146:149], v[142:145]
	v_mfma_f32_16x16x32_f16 v[142:145], v[82:85], v[150:153], v[142:145]
	v_mfma_f32_16x16x32_f16 v[142:145], v[90:93], v[154:157], v[142:145]
	v_mfma_f32_16x16x32_f16 v[142:145], v[98:101], v[158:161], v[142:145]
	v_mfma_f32_16x16x32_f16 v[142:145], v[106:109], v[208:211], v[142:145]
	v_mfma_f32_16x16x32_f16 v[142:145], v[114:117], v[212:215], v[142:145]
	v_mfma_f32_16x16x32_f16 v[142:145], v[122:125], v[216:219], v[142:145]
	v_mfma_f32_16x16x32_f16 v[142:145], v[10:13], v[220:223], v[142:145]
	v_mul_f32_e32 v236, 0xb6b8aa3b, v138
	v_mul_f32_e32 v237, 0xb6b8aa3b, v139
	v_mul_f32_e32 v238, 0x3738aa3b, v140
	v_mul_f32_e32 v239, 0xb6b8aa3b, v141
	v_exp_f32_e32 v236, v236
	v_exp_f32_e32 v237, v237
	v_exp_f32_e32 v238, v238
	v_exp_f32_e32 v239, v239
	s_add_i32 s44, s43, 1
	v_add_f32_e32 v236, 1.0, v236
	v_add_f32_e32 v237, 1.0, v237
	v_add_f32_e32 v238, 1.0, v238
	v_add_f32_e32 v239, 1.0, v239
	v_rcp_f32_e32 v236, v236
	v_rcp_f32_e32 v237, v237
	v_rcp_f32_e32 v238, v238
	v_rcp_f32_e32 v239, v239
	v_cmp_eq_u32_e32 vcc, 0, v190
	s_lshl_b32 s6, s44, 15
	v_fma_f32 v238, v238, -2.0, 1.0
	s_and_b32 s6, s6, 0x8000
	v_cndmask_b32_e64 v240, v188, 0, vcc
	v_mul_f32_e32 v236, v236, v238
	v_fma_f32 v188, v240, v237, v236
	v_mul_f32_e32 v241, 0x4038aa3b, v188
	v_exp_f32_e32 v241, v241
	s_add_u32 s6, s33, s6
	s_addc_u32 s7, s35, 0
	v_add_f32_e32 v241, 1.0, v241
	v_rcp_f32_e32 v241, v241
	v_lshlrev_b32_e32 v166, 3, v184
	v_fma_f32 v241, v241, -2.0, 1.0
	v_mul_f32_e32 v241, v239, v241
	v_mul_f32_e32 v242, 0xb6b8aa3b, v142
	v_mul_f32_e32 v243, 0xb6b8aa3b, v143
	v_mul_f32_e32 v244, 0x3738aa3b, v144
	v_mul_f32_e32 v245, 0xb6b8aa3b, v145
	v_exp_f32_e32 v242, v242
	v_exp_f32_e32 v243, v243
	v_exp_f32_e32 v244, v244
	v_exp_f32_e32 v245, v245
	s_and_b64 s[8:9], s[20:21], s[4:5]
	v_add_f32_e32 v242, 1.0, v242
	v_add_f32_e32 v243, 1.0, v243
	v_add_f32_e32 v244, 1.0, v244
	v_add_f32_e32 v245, 1.0, v245
	v_rcp_f32_e32 v242, v242
	v_rcp_f32_e32 v243, v243
	v_rcp_f32_e32 v244, v244
	v_rcp_f32_e32 v245, v245
	v_cndmask_b32_e64 v246, v189, 0, vcc
	v_fma_f32 v244, v244, -2.0, 1.0
	v_mov_b32_e32 v138, v240
	v_mul_f32_e32 v242, v242, v244
	v_fma_f32 v189, v246, v243, v242
	v_mul_f32_e32 v247, 0x4038aa3b, v189
	v_exp_f32_e32 v247, v247
	v_mov_b32_e32 v139, v246
	v_mov_b32_e32 v142, v241
	v_add_f32_e32 v247, 1.0, v247
	v_rcp_f32_e32 v247, v247
	v_mov_b32_e32 v143, s44
	v_fma_f32 v247, v247, -2.0, 1.0
	v_mov_b32_e32 v141, s44
	v_mul_f32_e32 v140, v245, v247
	s_andn2_b64 vcc, exec, s[8:9]
	s_mov_b64 s[8:9], -1
	s_cbranch_vccnz .LBB1_30
	s_branch .Lgates_tail

.Lgates_sum:
	v_mul_f32_e32 v154, 0xb6b8aa3b, v154
	v_mul_f32_e32 v155, 0xb6b8aa3b, v155
	v_mul_f32_e32 v156, 0x3738aa3b, v156
	v_mul_f32_e32 v146, 0xb6b8aa3b, v146
	v_mul_f32_e32 v147, 0xb6b8aa3b, v147
	v_mul_f32_e32 v148, 0x3738aa3b, v148
	v_mul_f32_e32 v157, 0xb6b8aa3b, v157
	v_mul_f32_e32 v149, 0xb6b8aa3b, v149
	v_exp_f32_e32 v154, v154
	v_exp_f32_e32 v155, v155
	v_exp_f32_e32 v156, v156
	v_exp_f32_e32 v146, v146
	v_exp_f32_e32 v147, v147
	v_exp_f32_e32 v148, v148
	v_exp_f32_e32 v157, v157
	v_exp_f32_e32 v149, v149
	s_add_i32 s44, s43, 1
	v_add_f32_e32 v154, 1.0, v154
	v_add_f32_e32 v155, 1.0, v155
	v_add_f32_e32 v156, 1.0, v156
	v_add_f32_e32 v146, 1.0, v146
	v_add_f32_e32 v147, 1.0, v147
	v_add_f32_e32 v148, 1.0, v148
	v_add_f32_e32 v157, 1.0, v157
	v_add_f32_e32 v149, 1.0, v149
	v_rcp_f32_e32 v154, v154
	v_rcp_f32_e32 v155, v155
	v_rcp_f32_e32 v156, v156
	v_rcp_f32_e32 v146, v146
	v_rcp_f32_e32 v147, v147
	v_rcp_f32_e32 v148, v148
	v_rcp_f32_e32 v157, v157
	v_rcp_f32_e32 v149, v149
	v_cmp_eq_u32_e32 vcc, 0, v190
	v_fma_f32 v156, v156, -2.0, 1.0
	v_fma_f32 v148, v148, -2.0, 1.0
	s_lshl_b32 s6, s44, 15
	v_cndmask_b32_e64 v138, v188, 0, vcc
	v_cndmask_b32_e64 v139, v189, 0, vcc
	s_and_b32 s6, s6, 0x8000
	v_mul_f32_e32 v154, v154, v156
	v_mul_f32_e32 v146, v146, v148
	s_add_u32 s6, s33, s6
	v_fma_f32 v188, v138, v155, v154
	v_fma_f32 v189, v139, v147, v146
	s_addc_u32 s7, s35, 0
	v_mul_f32_e32 v140, 0x4038aa3b, v188
	v_mul_f32_e32 v141, 0x4038aa3b, v189
	v_exp_f32_e32 v140, v140
	v_exp_f32_e32 v141, v141
	v_lshlrev_b32_e32 v166, 3, v184
	v_add_f32_e32 v140, 1.0, v140
	v_add_f32_e32 v141, 1.0, v141
	v_rcp_f32_e32 v140, v140
	v_rcp_f32_e32 v141, v141
	v_fma_f32 v140, v140, -2.0, 1.0
	v_fma_f32 v141, v141, -2.0, 1.0
	s_and_b64 s[8:9], s[20:21], s[4:5]
	v_mul_f32_e32 v142, v157, v140
	v_mul_f32_e32 v140, v149, v141
	v_mov_b32_e32 v143, s44
	v_mov_b32_e32 v141, s44
	s_andn2_b64 vcc, exec, s[8:9]
	s_mov_b64 s[8:9], -1
	s_cbranch_vccnz .LBB1_30
.Lgates_tail:
	s_andn2_b64 vcc, exec, s[8:9]
	s_cbranch_vccz .LBB1_31

.LBB1_30:
	global_store_dwordx2 v234, v[142:143], s[6:7] sc1
	global_store_dwordx2 v234, v[140:141], s[6:7] offset:512 sc1
	s_cbranch_execnz .LBB1_28
.LBB1_31:
	global_store_dwordx2 v234, v[142:143], s[6:7] sc0
	global_store_dwordx2 v234, v[140:141], s[6:7] offset:512 sc0
	s_cmp_lt_u32 s43, 32
	s_cbranch_scc1 .LBB1_29

	.amdhsa_kernel _Z11lstm_kernel2LP
		.amdhsa_group_segment_fixed_size 38152
		.amdhsa_private_segment_fixed_size 0
		.amdhsa_kernarg_size 336
		.amdhsa_user_sgpr_count 2
		.amdhsa_user_sgpr_dispatch_ptr 0
		.amdhsa_user_sgpr_queue_ptr 0
		.amdhsa_user_sgpr_kernarg_segment_ptr 1
		.amdhsa_user_sgpr_dispatch_id 0
		.amdhsa_user_sgpr_kernarg_preload_length 0
		.amdhsa_user_sgpr_kernarg_preload_offset 0
		.amdhsa_user_sgpr_private_segment_size 0
		.amdhsa_uses_dynamic_stack 0
		.amdhsa_enable_private_segment 0
		.amdhsa_system_sgpr_workgroup_id_x 1
		.amdhsa_system_sgpr_workgroup_id_y 0
		.amdhsa_system_sgpr_workgroup_id_z 0
		.amdhsa_system_sgpr_workgroup_info 0
		.amdhsa_system_vgpr_workitem_id 2
		.amdhsa_next_free_vgpr 248
		.amdhsa_next_free_sgpr 54
		.amdhsa_accum_offset 248
		.amdhsa_reserve_vcc 1
		.amdhsa_float_round_mode_32 0
		.amdhsa_float_round_mode_16_64 0
		.amdhsa_float_denorm_mode_32 3
		.amdhsa_float_denorm_mode_16_64 3
		.amdhsa_dx10_clamp 1
		.amdhsa_ieee_mode 1
		.amdhsa_fp16_overflow 0
		.amdhsa_tg_split 0
		.amdhsa_exception_fp_ieee_invalid_op 0
		.amdhsa_exception_fp_denorm_src 0
		.amdhsa_exception_fp_ieee_div_zero 0
		.amdhsa_exception_fp_ieee_overflow 0
		.amdhsa_exception_fp_ieee_underflow 0
		.amdhsa_exception_fp_ieee_inexact 0
		.amdhsa_exception_int_div_zero 0
	.end_amdhsa_kernel

amdhsa.kernels:
  - .agpr_count:     0
    .args:
      - .actual_access:  read_only
        .address_space:  global
        .offset:         0
        .size:           8
        .value_kind:     global_buffer
      - .actual_access:  read_only
        .address_space:  global
        .offset:         8
        .size:           8
        .value_kind:     global_buffer
      - .actual_access:  read_only
        .address_space:  global
        .offset:         16
        .size:           8
        .value_kind:     global_buffer
      - .actual_access:  read_only
        .address_space:  global
        .offset:         24
        .size:           8
        .value_kind:     global_buffer
      - .actual_access:  read_only
        .address_space:  global
        .offset:         32
        .size:           8
        .value_kind:     global_buffer
      - .actual_access:  read_only
        .address_space:  global
        .offset:         40
        .size:           8
        .value_kind:     global_buffer
      - .actual_access:  read_only
        .address_space:  global
        .offset:         48
        .size:           8
        .value_kind:     global_buffer
      - .actual_access:  read_only
        .address_space:  global
        .offset:         56
        .size:           8
        .value_kind:     global_buffer
      - .actual_access:  write_only
        .address_space:  global
        .offset:         64
        .size:           8
        .value_kind:     global_buffer
      - .actual_access:  write_only
        .address_space:  global
        .offset:         72
        .size:           8
        .value_kind:     global_buffer
      - .offset:         80
        .size:           4
        .value_kind:     by_value
      - .actual_access:  read_only
        .address_space:  global
        .offset:         88
        .size:           8
        .value_kind:     global_buffer
      - .actual_access:  read_only
        .address_space:  global
        .offset:         96
        .size:           8
        .value_kind:     global_buffer
    .group_segment_fixed_size: 147456
    .kernarg_segment_align: 8
    .kernarg_segment_size: 104
    .language:       OpenCL C
    .language_version:
      - 2
      - 0
    .max_flat_workgroup_size: 512
    .name:           _Z13xg_gemm_f16x3PKiPKfS2_S2_S2_S2_S2_S2_PfPDv4_fiS2_S2_
    .private_segment_fixed_size: 0
    .sgpr_count:     36
    .sgpr_spill_count: 0
    .symbol:         _Z13xg_gemm_f16x3PKiPKfS2_S2_S2_S2_S2_S2_PfPDv4_fiS2_S2_.kd
    .uniform_work_group_size: 1
    .uses_dynamic_stack: false
    .vgpr_count:     242
    .vgpr_spill_count: 0
    .wavefront_size: 64
  - .agpr_count:     0
    .args:
      - .offset:         0
        .size:           80
        .value_kind:     by_value
      - .offset:         80
        .size:           4
        .value_kind:     hidden_block_count_x
      - .offset:         84
        .size:           4
        .value_kind:     hidden_block_count_y
      - .offset:         88
        .size:           4
        .value_kind:     hidden_block_count_z
      - .offset:         92
        .size:           2
        .value_kind:     hidden_group_size_x
      - .offset:         94
        .size:           2
        .value_kind:     hidden_group_size_y
      - .offset:         96
        .size:           2
        .value_kind:     hidden_group_size_z
      - .offset:         98
        .size:           2
        .value_kind:     hidden_remainder_x
      - .offset:         100
        .size:           2
        .value_kind:     hidden_remainder_y
      - .offset:         102
        .size:           2
        .value_kind:     hidden_remainder_z
      - .offset:         120
        .size:           8
        .value_kind:     hidden_global_offset_x
      - .offset:         128
        .size:           8
        .value_kind:     hidden_global_offset_y
      - .offset:         136
        .size:           8
        .value_kind:     hidden_global_offset_z
      - .offset:         144
        .size:           2
        .value_kind:     hidden_grid_dims
    .group_segment_fixed_size: 38152
    .kernarg_segment_align: 8
    .kernarg_segment_size: 336
    .language:       OpenCL C
    .language_version:
      - 2
      - 0
    .max_flat_workgroup_size: 512
    .name:           _Z11lstm_kernel2LP
    .private_segment_fixed_size: 0
    .sgpr_count:     60
    .sgpr_spill_count: 0
    .symbol:         _Z11lstm_kernel2LP.kd
    .uniform_work_group_size: 1
    .uses_dynamic_stack: false
    .vgpr_count:     248
    .vgpr_spill_count: 0
    .wavefront_size: 64
  - .agpr_count:     0
    .args:
      - .actual_access:  read_only
        .address_space:  global
        .offset:         0
        .size:           8
        .value_kind:     global_buffer
      - .actual_access:  read_only
        .address_space:  global
        .offset:         8
        .size:           8
        .value_kind:     global_buffer
      - .actual_access:  read_only
        .address_space:  global
        .offset:         16
        .size:           8
        .value_kind:     global_buffer
      - .actual_access:  write_only
        .address_space:  global
        .offset:         24
        .size:           8
        .value_kind:     global_buffer
    .group_segment_fixed_size: 0
    .kernarg_segment_align: 8
    .kernarg_segment_size: 32
    .language:       OpenCL C
    .language_version:
      - 2
      - 0
    .max_flat_workgroup_size: 256
    .name:           _Z12feats_kernelPKfS0_S0_Pd
    .private_segment_fixed_size: 0
    .sgpr_count:     14
    .sgpr_spill_count: 0
    .symbol:         _Z12feats_kernelPKfS0_S0_Pd.kd
    .uniform_work_group_size: 1
    .uses_dynamic_stack: false
    .vgpr_count:     116
    .vgpr_spill_count: 0
    .wavefront_size: 64
  - .agpr_count:     0
    .args:
      - .actual_access:  read_only
        .address_space:  global
        .offset:         0
        .size:           8
        .value_kind:     global_buffer
      - .actual_access:  read_only
        .address_space:  global
        .offset:         8
        .size:           8
        .value_kind:     global_buffer
      - .actual_access:  write_only
        .address_space:  global
        .offset:         16
        .size:           8
        .value_kind:     global_buffer
      - .actual_access:  write_only
        .address_space:  global
        .offset:         24
        .size:           8
        .value_kind:     global_buffer
    .group_segment_fixed_size: 19200
    .kernarg_segment_align: 8
    .kernarg_segment_size: 32
    .language:       OpenCL C
    .language_version:
      - 2
      - 0
    .max_flat_workgroup_size: 768
    .name:           _Z11vitA_kernelPKdPKfPdS3_
    .private_segment_fixed_size: 0
    .sgpr_count:     18
    .sgpr_spill_count: 0
    .symbol:         _Z11vitA_kernelPKdPKfPdS3_.kd
    .uniform_work_group_size: 1
    .uses_dynamic_stack: false
    .vgpr_count:     76
    .vgpr_spill_count: 0
    .wavefront_size: 64
  - .agpr_count:     0
    .args:
      - .actual_access:  read_only
        .address_space:  global
        .offset:         0
        .size:           8
        .value_kind:     global_buffer
      - .actual_access:  write_only
        .address_space:  global
        .offset:         8
        .size:           8
        .value_kind:     global_buffer
      - .actual_access:  write_only
        .address_space:  global
        .offset:         16
        .size:           8
        .value_kind:     global_buffer
      - .actual_access:  write_only
        .address_space:  global
        .offset:         24
        .size:           8
        .value_kind:     global_buffer
    .group_segment_fixed_size: 16128
    .kernarg_segment_align: 8
    .kernarg_segment_size: 32
    .language:       OpenCL C
    .language_version:
      - 2
      - 0
    .max_flat_workgroup_size: 576
    .name:           _Z12vitB1_kernelPKdPdS1_S1_
    .private_segment_fixed_size: 0
    .sgpr_count:     18
    .sgpr_spill_count: 0
    .symbol:         _Z12vitB1_kernelPKdPdS1_S1_.kd
    .uniform_work_group_size: 1
    .uses_dynamic_stack: false
    .vgpr_count:     59
    .vgpr_spill_count: 0
    .wavefront_size: 64
  - .agpr_count:     0
    .args:
      - .actual_access:  read_only
        .address_space:  global
        .offset:         0
        .size:           8
        .value_kind:     global_buffer
      - .actual_access:  read_only
        .address_space:  global
        .offset:         8
        .size:           8
        .value_kind:     global_buffer
      - .actual_access:  read_only
        .address_space:  global
        .offset:         16
        .size:           8
        .value_kind:     global_buffer
      - .actual_access:  read_only
        .address_space:  global
        .offset:         24
        .size:           8
        .value_kind:     global_buffer
      - .actual_access:  write_only
        .address_space:  global
        .offset:         32
        .size:           8
        .value_kind:     global_buffer
    .group_segment_fixed_size: 16320
    .kernarg_segment_align: 8
    .kernarg_segment_size: 40
    .language:       OpenCL C
    .language_version:
      - 2
      - 0
    .max_flat_workgroup_size: 1024
    .name:           _Z12vitB2_kernelPKdS0_S0_S0_Pd
    .private_segment_fixed_size: 0
    .sgpr_count:     42
    .sgpr_spill_count: 0
    .symbol:         _Z12vitB2_kernelPKdS0_S0_S0_Pd.kd
    .uniform_work_group_size: 1
    .uses_dynamic_stack: false
    .vgpr_count:     58
    .vgpr_spill_count: 0
    .wavefront_size: 64
  - .agpr_count:     0
    .args:
      - .actual_access:  read_only
        .address_space:  global
        .offset:         0
        .size:           8
        .value_kind:     global_buffer
      - .actual_access:  read_only
        .address_space:  global
        .offset:         8
        .size:           8
        .value_kind:     global_buffer
      - .actual_access:  read_only
        .address_space:  global
        .offset:         16
        .size:           8
        .value_kind:     global_buffer
      - .actual_access:  read_only
        .address_space:  global
        .offset:         24
        .size:           8
        .value_kind:     global_buffer
      - .actual_access:  write_only
        .address_space:  global
        .offset:         32
        .size:           8
        .value_kind:     global_buffer
      - .actual_access:  write_only
        .address_space:  global
        .offset:         40
        .size:           8
        .value_kind:     global_buffer
      - .actual_access:  write_only
        .address_space:  global
        .offset:         48
        .size:           8
        .value_kind:     global_buffer
    .group_segment_fixed_size: 0
    .kernarg_segment_align: 8
    .kernarg_segment_size: 56
    .language:       OpenCL C
    .language_version:
      - 2
      - 0
    .max_flat_workgroup_size: 64
    .name:           _Z11vitC_kernelPKdPKfS0_S0_PhPdS3_
    .private_segment_fixed_size: 0
    .sgpr_count:     34
    .sgpr_spill_count: 0
    .symbol:         _Z11vitC_kernelPKdPKfS0_S0_PhPdS3_.kd
    .uniform_work_group_size: 1
    .uses_dynamic_stack: false
    .vgpr_count:     86
    .vgpr_spill_count: 0
    .wavefront_size: 64
  - .agpr_count:     0
    .args:
      - .actual_access:  read_only
        .address_space:  global
        .offset:         0
        .size:           8
        .value_kind:     global_buffer
      - .actual_access:  read_only
        .address_space:  global
        .offset:         8
        .size:           8
        .value_kind:     global_buffer
      - .actual_access:  read_only
        .address_space:  global
        .offset:         16
        .size:           8
        .value_kind:     global_buffer
      - .actual_access:  read_only
        .address_space:  global
        .offset:         24
        .size:           8
        .value_kind:     global_buffer
      - .actual_access:  write_only
        .address_space:  global
        .offset:         32
        .size:           8
        .value_kind:     global_buffer
    .group_segment_fixed_size: 30424
    .kernarg_segment_align: 8
    .kernarg_segment_size: 40
    .language:       OpenCL C
    .language_version:
      - 2
      - 0
    .max_flat_workgroup_size: 1024
    .name:           _Z11vitD_kernelPKhPKdPKfS0_Pf
    .private_segment_fixed_size: 0
    .sgpr_count:     46
    .sgpr_spill_count: 0
    .symbol:         _Z11vitD_kernelPKhPKdPKfS0_Pf.kd
    .uniform_work_group_size: 1
    .uses_dynamic_stack: false
    .vgpr_count:     28
    .vgpr_spill_count: 0
    .wavefront_size: 64
